# mLSTM n-update: 32 serialized LDS round trips replaced by a 4-stage pipelined read (same fma order), on top of hosted conversion + group split
# speedup vs baseline: 1.0354x; 1.0157x over previous
; #define LAS __attribute__((address_space(3)))
; __device__ __forceinline__ unsigned cvt_pk_bf16(float lo, float hi) { unsigned r; asm volatile("v_cvt_pk_bf16_f32 %0, %1, %2" : "=v"(r) : "v"(lo), "v"(hi)); return r; }
; __device__ __forceinline__ void mlstm_unit(LAS unsigned char* lds, const bf16_t* __restrict__ PM, const float* __restrict__ GATES, bf16_t* __restrict__ Hout,
;                                            int b, int h, int dir, int vs, Conv& cvs, const int wave_) {
;     ...
;         {
;             const float wcv = *(LAS float*)(lds + SC_WC);
;             const int k0 = 32 * w;
; #pragma unroll
;             for (int a = 0; a < 2; ++a)
; #pragma unroll
;                 for (int v = 0; v < 4; ++v) accC[a][v] *= wcv;
; #pragma unroll
;             for (int s2 = 0; s2 < 2; ++s2) {
;                 bf16x8 A[2], B[4];
; #pragma unroll
;                 for (int a = 0; a < 2; ++a) A[a] = tr_pair(lds + KS + (32 * s2 + 8 * g + q4) * RQ + (k0 + 16 * a + 4 * p4) * 2, 4 * RQ);
; #pragma unroll
;                 for (int v = 0; v < 4; ++v) B[v] = tr_pair(lds + VWS + (32 * s2 + 8 * g + q4) * RV + (16 * v + 4 * p4) * 2, 4 * RV);
; #pragma unroll
;                 for (int a = 0; a < 2; ++a)
; #pragma unroll
;                     for (int v = 0; v < 4; ++v) accC[a][v] = __builtin_amdgcn_mfma_f32_16x16x32_bf16(A[a], B[v], accC[a][v], 0, 0, 0);
;             }
; #pragma unroll
;             for (int a = 0; a < 2; ++a)
; #pragma unroll
;                 for (int v = 0; v < 4; ++v) {
;                     u32x2 o; o.x = cvt_pk_bf16(accC[a][v][0], accC[a][v][1]); o.y = cvt_pk_bf16(accC[a][v][2], accC[a][v][3]);
;                     *(LAS u32x2*)(lds + CTS + (16 * v + i16) * RQ + (k0 + 16 * a + 4 * g) * 2) = o;
;                 }
.LBB0_615:
	v_mov_b32_e32 v132, s1
	v_add_u32_e32 v212, v164, v169
	ds_read_b32 v152, v132
	ds_read_b64_tr_b16 v[134:135], v191 offset:35904
	ds_read_b64_tr_b16 v[132:133], v191 offset:33792
	ds_read_b64_tr_b16 v[138:139], v212 offset:576
	ds_read_b64_tr_b16 v[136:137], v212
	ds_read_b64_tr_b16 v[202:203], v212 offset:32
	ds_read_b64_tr_b16 v[204:205], v212 offset:608
	ds_read_b64_tr_b16 v[206:207], v212 offset:64
	ds_read_b64_tr_b16 v[208:209], v212 offset:640
	ds_read_b64_tr_b16 v[210:211], v212 offset:96
	ds_read_b64_tr_b16 v[212:213], v212 offset:672
	ds_read_b64_tr_b16 v[214:215], v191 offset:33824
	ds_read_b64_tr_b16 v[216:217], v191 offset:35936
	s_waitcnt lgkmcnt(12)
	v_pk_mul_f32 v[50:51], v[50:51], v[152:153] op_sel_hi:[1,0]
	v_pk_mul_f32 v[48:49], v[48:49], v[152:153] op_sel_hi:[1,0]
	v_pk_mul_f32 v[46:47], v[46:47], v[152:153] op_sel_hi:[1,0]
	v_pk_mul_f32 v[44:45], v[44:45], v[152:153] op_sel_hi:[1,0]
	v_pk_mul_f32 v[42:43], v[42:43], v[152:153] op_sel_hi:[1,0]
	v_pk_mul_f32 v[40:41], v[40:41], v[152:153] op_sel_hi:[1,0]
	v_pk_mul_f32 v[38:39], v[38:39], v[152:153] op_sel_hi:[1,0]
	v_pk_mul_f32 v[36:37], v[36:37], v[152:153] op_sel_hi:[1,0]
	v_pk_mul_f32 v[66:67], v[66:67], v[152:153] op_sel_hi:[1,0]
	v_pk_mul_f32 v[64:65], v[64:65], v[152:153] op_sel_hi:[1,0]
	v_pk_mul_f32 v[54:55], v[54:55], v[152:153] op_sel_hi:[1,0]
	v_pk_mul_f32 v[52:53], v[52:53], v[152:153] op_sel_hi:[1,0]
	v_pk_mul_f32 v[58:59], v[58:59], v[152:153] op_sel_hi:[1,0]
	v_pk_mul_f32 v[56:57], v[56:57], v[152:153] op_sel_hi:[1,0]
	v_pk_mul_f32 v[62:63], v[62:63], v[152:153] op_sel_hi:[1,0]
	v_pk_mul_f32 v[60:61], v[60:61], v[152:153] op_sel_hi:[1,0]
	s_waitcnt lgkmcnt(8)
	v_mfma_f32_16x16x32_bf16 v[48:51], v[132:135], v[136:139], v[48:51]
	s_waitcnt lgkmcnt(6)
	v_mfma_f32_16x16x32_bf16 v[44:47], v[132:135], v[202:205], v[44:47]
	s_waitcnt lgkmcnt(4)
	v_mfma_f32_16x16x32_bf16 v[40:43], v[132:135], v[206:209], v[40:43]
	s_waitcnt lgkmcnt(2)
	v_mfma_f32_16x16x32_bf16 v[36:39], v[132:135], v[210:213], v[36:39]
	s_waitcnt lgkmcnt(0)
	v_mfma_f32_16x16x32_bf16 v[64:67], v[214:217], v[136:139], v[64:67]
	v_mfma_f32_16x16x32_bf16 v[52:55], v[214:217], v[202:205], v[52:55]
	ds_read_b64_tr_b16 v[202:203], v191 offset:50688
	ds_read_b64_tr_b16 v[204:205], v191 offset:52800
	v_mfma_f32_16x16x32_bf16 v[56:59], v[214:217], v[206:209], v[56:59]
	v_mfma_f32_16x16x32_bf16 v[60:63], v[214:217], v[210:213], v[60:63]
	ds_read_b64_tr_b16 v[208:209], v192 offset:576
	ds_read_b64_tr_b16 v[206:207], v192
	ds_read_b64_tr_b16 v[210:211], v192 offset:32
	ds_read_b64_tr_b16 v[212:213], v192 offset:608
	ds_read_b64_tr_b16 v[214:215], v192 offset:64
	ds_read_b64_tr_b16 v[216:217], v192 offset:640
	ds_read_b64_tr_b16 v[132:133], v192 offset:96
	ds_read_b64_tr_b16 v[134:135], v192 offset:672
	ds_read_b64_tr_b16 v[136:137], v191 offset:50720
	ds_read_b64_tr_b16 v[138:139], v191 offset:52832
	s_waitcnt lgkmcnt(8)
	v_mfma_f32_16x16x32_bf16 v[48:51], v[202:205], v[206:209], v[48:51]
	s_waitcnt lgkmcnt(6)
	v_mfma_f32_16x16x32_bf16 v[44:47], v[202:205], v[210:213], v[44:47]
	s_waitcnt lgkmcnt(4)
	v_mfma_f32_16x16x32_bf16 v[40:43], v[202:205], v[214:217], v[40:43]
	s_waitcnt lgkmcnt(2)
	v_mfma_f32_16x16x32_bf16 v[36:39], v[202:205], v[132:135], v[36:39]
	v_cvt_pk_bf16_f32 v202, v48, v49
	v_cvt_pk_bf16_f32 v203, v50, v51
	ds_write_b64 v193, v[202:203]
	v_cvt_pk_bf16_f32 v202, v44, v45
	s_waitcnt lgkmcnt(1)
; #define LAS __attribute__((address_space(3)))
; __device__ __forceinline__ unsigned cvt_pk_bf16(float lo, float hi) { unsigned r; asm volatile("v_cvt_pk_bf16_f32 %0, %1, %2" : "=v"(r) : "v"(lo), "v"(hi)); return r; }
; __device__ __forceinline__ float bf_s(unsigned short h) { return __uint_as_float(((unsigned)h) << 16); }
; __device__ __forceinline__ void mlstm_unit(LAS unsigned char* lds, const bf16_t* __restrict__ PM, const float* __restrict__ GATES, bf16_t* __restrict__ Hout,
;                                            int b, int h, int dir, int vs, Conv& cvs, const int wave_) {
;     ...
; #pragma unroll
;             for (int a = 0; a < 2; ++a)
; #pragma unroll
;                 for (int v = 0; v < 4; ++v) {
;                     u32x2 o; o.x = cvt_pk_bf16(accC[a][v][0], accC[a][v][1]); o.y = cvt_pk_bf16(accC[a][v][2], accC[a][v][3]);
;                     *(LAS u32x2*)(lds + CTS + (16 * v + i16) * RQ + (k0 + 16 * a + 4 * g) * 2) = o;
;                 }
;             {
;                 const int kk_ = tid & 255, hf_ = tid >> 8;
;                 float nv = hf_ ? 0.f : wcv * *(LAS float*)(lds + NV + kk_ * 4);
; #pragma unroll 8
;                 for (int s = 0; s < 32; ++s) nv += *(LAS float*)(lds + SC_WS + (hf_ * 32 + s) * 4) * bf_s(*(const LAS unsigned short*)(lds + KS + (hf_ * 32 + s) * RQ + kk_ * 2));
;                 *(LAS float*)(lds + (hf_ ? NV2 : NV) + kk_ * 4) = nv;
;             }
;         }
;         __syncthreads();
	v_mfma_f32_16x16x32_bf16 v[60:63], v[136:139], v[132:135], v[60:63]
	v_cvt_pk_bf16_f32 v203, v46, v47
	ds_write_b64 v193, v[202:203] offset:8448
	v_cvt_pk_bf16_f32 v132, v40, v41
	v_cvt_pk_bf16_f32 v133, v42, v43
	ds_write_b64 v193, v[132:133] offset:16896
	v_cvt_pk_bf16_f32 v132, v36, v37
	v_mfma_f32_16x16x32_bf16 v[64:67], v[136:139], v[206:209], v[64:67]
	v_cvt_pk_bf16_f32 v133, v38, v39
	ds_write_b64 v193, v[132:133] offset:25344
	v_cvt_pk_bf16_f32 v132, v64, v65
	v_mfma_f32_16x16x32_bf16 v[52:55], v[136:139], v[210:213], v[52:55]
	v_cvt_pk_bf16_f32 v133, v66, v67
	ds_write_b64 v193, v[132:133] offset:32
	v_cvt_pk_bf16_f32 v132, v52, v53
	v_mfma_f32_16x16x32_bf16 v[56:59], v[136:139], v[214:217], v[56:59]
	v_cvt_pk_bf16_f32 v133, v54, v55
	ds_write_b64 v193, v[132:133] offset:8480
	v_cvt_pk_bf16_f32 v132, v56, v57
	v_cvt_pk_bf16_f32 v133, v58, v59
	ds_write_b64 v193, v[132:133] offset:16928
	v_cvt_pk_bf16_f32 v132, v60, v61
	v_cvt_pk_bf16_f32 v133, v62, v63
	ds_write_b64 v193, v[132:133] offset:25376
	v_mov_b32_e32 v134, 0
	s_and_saveexec_b64 s[2:3], s[12:13]
	ds_read_b32 v134, v201
	s_or_b64 exec, exec, s[2:3]
	v_add_u32_e32 v133, 0x20000, v181
	ds_read_b128 v[202:205], v133
	ds_read_b128 v[206:209], v133 offset:16
	ds_read_u16 v218, v179
	ds_read_u16 v219, v179 offset:528
	ds_read_u16 v220, v179 offset:1056
	ds_read_u16 v221, v179 offset:1584
	ds_read_u16 v222, v179 offset:2112
	ds_read_u16 v223, v179 offset:2640
	ds_read_u16 v224, v179 offset:3168
	ds_read_u16 v225, v179 offset:3696
	ds_read_b128 v[210:213], v133 offset:32
	ds_read_b128 v[214:217], v133 offset:48
	ds_read_u16 v226, v179 offset:4224
	ds_read_u16 v227, v179 offset:4752
	ds_read_u16 v228, v179 offset:5280
	ds_read_u16 v229, v179 offset:5808
	ds_read_u16 v230, v179 offset:6336
	ds_read_u16 v231, v179 offset:6864
	ds_read_u16 v232, v179 offset:7392
	ds_read_u16 v233, v179 offset:7920
	s_waitcnt lgkmcnt(10)
	v_mul_f32_e32 v132, v152, v134
	v_lshlrev_b32_e32 v218, 16, v218
	v_fmac_f32_e32 v132, v202, v218
	v_lshlrev_b32_e32 v219, 16, v219
	v_fmac_f32_e32 v132, v203, v219
	v_lshlrev_b32_e32 v220, 16, v220
	v_fmac_f32_e32 v132, v204, v220
	v_lshlrev_b32_e32 v221, 16, v221
	v_fmac_f32_e32 v132, v205, v221
	v_lshlrev_b32_e32 v222, 16, v222
	v_fmac_f32_e32 v132, v206, v222
	v_lshlrev_b32_e32 v223, 16, v223
	v_fmac_f32_e32 v132, v207, v223
	v_lshlrev_b32_e32 v224, 16, v224
	v_fmac_f32_e32 v132, v208, v224
	v_lshlrev_b32_e32 v225, 16, v225
	v_fmac_f32_e32 v132, v209, v225
	ds_read_b128 v[202:205], v133 offset:64
	ds_read_b128 v[206:209], v133 offset:80
	ds_read_u16 v218, v179 offset:8448
	ds_read_u16 v219, v179 offset:8976
	ds_read_u16 v220, v179 offset:9504
	ds_read_u16 v221, v179 offset:10032
	ds_read_u16 v222, v179 offset:10560
	ds_read_u16 v223, v179 offset:11088
	ds_read_u16 v224, v179 offset:11616
	ds_read_u16 v225, v179 offset:12144
	s_waitcnt lgkmcnt(10)
	v_lshlrev_b32_e32 v226, 16, v226
	v_fmac_f32_e32 v132, v210, v226
	v_lshlrev_b32_e32 v227, 16, v227
	v_fmac_f32_e32 v132, v211, v227
	v_lshlrev_b32_e32 v228, 16, v228
	v_fmac_f32_e32 v132, v212, v228
	v_lshlrev_b32_e32 v229, 16, v229
	v_fmac_f32_e32 v132, v213, v229
	v_lshlrev_b32_e32 v230, 16, v230
	v_fmac_f32_e32 v132, v214, v230
	v_lshlrev_b32_e32 v231, 16, v231
	v_fmac_f32_e32 v132, v215, v231
	v_lshlrev_b32_e32 v232, 16, v232
	v_fmac_f32_e32 v132, v216, v232
	v_lshlrev_b32_e32 v233, 16, v233
	v_fmac_f32_e32 v132, v217, v233
	ds_read_b128 v[210:213], v133 offset:96
	ds_read_b128 v[214:217], v133 offset:112
	ds_read_u16 v226, v179 offset:12672
	ds_read_u16 v227, v179 offset:13200
	ds_read_u16 v228, v179 offset:13728
	ds_read_u16 v229, v179 offset:14256
	ds_read_u16 v230, v179 offset:14784
	ds_read_u16 v231, v179 offset:15312
	ds_read_u16 v232, v179 offset:15840
	ds_read_u16 v233, v179 offset:16368
	s_waitcnt lgkmcnt(10)
	v_lshlrev_b32_e32 v218, 16, v218
	v_fmac_f32_e32 v132, v202, v218
	v_lshlrev_b32_e32 v219, 16, v219
	v_fmac_f32_e32 v132, v203, v219
	v_lshlrev_b32_e32 v220, 16, v220
	v_fmac_f32_e32 v132, v204, v220
	v_lshlrev_b32_e32 v221, 16, v221
	v_fmac_f32_e32 v132, v205, v221
	v_lshlrev_b32_e32 v222, 16, v222
	v_fmac_f32_e32 v132, v206, v222
	v_lshlrev_b32_e32 v223, 16, v223
	v_fmac_f32_e32 v132, v207, v223
	v_lshlrev_b32_e32 v224, 16, v224
	v_fmac_f32_e32 v132, v208, v224
	v_lshlrev_b32_e32 v225, 16, v225
	v_fmac_f32_e32 v132, v209, v225
	s_waitcnt lgkmcnt(0)
	v_lshlrev_b32_e32 v226, 16, v226
	v_fmac_f32_e32 v132, v210, v226
	v_lshlrev_b32_e32 v227, 16, v227
	v_fmac_f32_e32 v132, v211, v227
	v_lshlrev_b32_e32 v228, 16, v228
	v_fmac_f32_e32 v132, v212, v228
	v_lshlrev_b32_e32 v229, 16, v229
	v_fmac_f32_e32 v132, v213, v229
	v_lshlrev_b32_e32 v230, 16, v230
	v_fmac_f32_e32 v132, v214, v230
	v_lshlrev_b32_e32 v231, 16, v231
	v_fmac_f32_e32 v132, v215, v231
	v_lshlrev_b32_e32 v232, 16, v232
	v_fmac_f32_e32 v132, v216, v232
	v_lshlrev_b32_e32 v233, 16, v233
	v_fmac_f32_e32 v132, v217, v233
	s_cmp_eq_u32 s57, 36
	ds_write_b32 v194, v132
	s_waitcnt lgkmcnt(0)
	s_barrier
	s_cbranch_scc1 .LBB0_621
	s_mov_b32 s0, s57
	s_lshl_b32 s34, s0, 6
	s_cmp_gt_u32 s0, 3
	s_mov_b64 s[2:3], -1
	s_cbranch_scc1 .LBB0_539
	s_branch .LBB0_540
